# indexer item loop: next item's K and q_lin fragment loads issued before the score stores, stores left in flight across the barrier (counted vmcnt), Ws written before the epilogue
# speedup vs baseline: 1.0052x; 1.0052x over previous
; #define LAS __attribute__((address_space(3)))
; #define IDX_DECODE(it_, q0_, seg_, nadm_) do { int g_ = 0; while (32 * (g_ + 1) * (g_ + 2) / 2 <= (it_)) ++g_; \
;             const int rem_ = (it_) - 32 * g_ * (g_ + 1) / 2, nseg_ = g_ + 1; q0_ = (g_ * 32 + rem_ / nseg_) * 32; seg_ = rem_ % nseg_; nadm_ = (q0_ / 64 + 1) * 64; } while (0)
; #define IDX_STAGE_Q(b_, q0_) do { const bf16_t* qsrc_ = QI + (size_t)(q0_) * 1024; _Pragma("unroll") for (int i_ = 0; i_ < 8; ++i_) \
;             pg8::glds16_s((const void*)qsrc_, (unsigned)((lane & 31) * 2048 + (2 * wave + 16 * i_ + (lane >> 5)) * 16), ldsb3 + (unsigned)(b_) * 65536u + (unsigned)(2 * wave + 16 * i_) * 512u); } while (0)
; __global__ void __launch_bounds__(NTHREADS, 2) mega_fwd(Args args) {
;     ...
;         const unsigned ldsb3 = (unsigned)(uintptr_t)F.lds;
;         LAS float* const Wsb = (LAS float*)(F.lds + RING_BYTES + 1024);
;         int it = blockIdx.x, buf = 0, q0 = 0, seg = 0, nadm = 0;
;         __syncthreads();
;         if (it < NITEM) { IDX_DECODE(it, q0, seg, nadm); IDX_STAGE_Q(0, q0); Wsb[(tid >> 5) * 32 + (tid & 31)] = WI[(size_t)(q0 + (tid & 31)) * 16 + (tid >> 5)]; }
.LBB0_645:
	s_add_i32 s2, s0, 3
	s_mul_i32 s2, s1, s2
	s_add_i32 s0, s0, 1
	s_add_i32 s1, s1, 32
	s_lshr_b32 s2, s2, 1
	s_cmp_le_i32 s2, s29
	s_cbranch_scc1 .LBB0_645
	s_add_i32 s10, s0, 1
	v_cvt_f32_u32_e32 v2, s10
	s_lshl_b32 s1, s0, 5
	s_not_b32 s0, s0
	s_mul_i32 s2, s1, s10
	v_rcp_iflag_f32_e32 v2, v2
	s_lshr_b32 s2, s2, 1
	s_sub_i32 s11, s29, s2
	s_abs_i32 s3, s11
	v_mul_f32_e32 v2, 0x4f7ffffe, v2
	v_cvt_u32_f32_e32 v2, v2
	s_ashr_i32 s2, s11, 31
	v_readlane_b32 s14, v241, 5
	v_readlane_b32 s15, v241, 6
	v_readfirstlane_b32 s6, v2
	s_mul_i32 s0, s0, s6
	s_mul_hi_u32 s0, s6, s0
	s_add_i32 s6, s6, s0
	s_mul_hi_u32 s0, s3, s6
	s_mul_i32 s6, s0, s10
	s_sub_i32 s3, s3, s6
	s_add_i32 s6, s0, 1
	s_sub_i32 s7, s3, s10
	s_cmp_ge_u32 s3, s10
	s_cselect_b32 s0, s6, s0
	s_cselect_b32 s3, s7, s3
	s_add_i32 s6, s0, 1
	s_cmp_ge_u32 s3, s10
	s_cselect_b32 s0, s6, s0
	s_xor_b32 s0, s0, s2
	s_sub_i32 s12, s0, s2
	s_add_i32 s13, s12, s1
	s_lshl_b32 s0, s13, 5
	s_add_u32 s16, s14, 0x51500000
	s_addc_u32 s17, s15, 0
	s_ashr_i32 s1, s0, 31
	s_lshl_b64 s[2:3], s[0:1], 11
	s_add_u32 s2, s16, s2
	v_readlane_b32 s26, v241, 43
	v_lshrrev_b32_e32 v5, 5, v146
	s_addc_u32 s3, s17, s3
	v_lshlrev_b32_e32 v2, 11, v0
	s_lshl_b32 s6, s26, 1
	s_lshl_b32 s1, s26, 10
	v_and_b32_e32 v2, 0xf800, v2
	v_or_b32_e32 v3, s6, v5
	s_add_i32 s7, s1, 0
	v_lshl_add_u32 v147, v3, 4, v2
	s_mov_b32 s8, m0
	s_mov_b32 m0, s7
	s_nop 0
	global_load_lds_dwordx4 v147, s[2:3]
	s_mov_b32 m0, s8
	s_add_i32 s7, s6, 16
	s_lshl_b32 s18, s7, 9
	v_or_b32_e32 v3, s7, v5
	s_add_i32 s7, s18, 0
	v_lshl_add_u32 v222, v3, 4, v2
	s_mov_b32 s8, m0
	s_mov_b32 m0, s7
	s_nop 0
	global_load_lds_dwordx4 v222, s[2:3]
	s_mov_b32 m0, s8
	s_add_i32 s7, s6, 32
	s_lshl_b32 s19, s7, 9
	v_or_b32_e32 v3, s7, v5
	s_add_i32 s7, s19, 0
	v_lshl_add_u32 v223, v3, 4, v2
	s_mov_b32 s8, m0
	s_mov_b32 m0, s7
	s_nop 0
	global_load_lds_dwordx4 v223, s[2:3]
	s_mov_b32 m0, s8
	s_add_i32 s7, s6, 48
	s_lshl_b32 s20, s7, 9
	v_or_b32_e32 v3, s7, v5
	s_add_i32 s7, s20, 0
	v_lshl_add_u32 v224, v3, 4, v2
	s_mov_b32 s8, m0
	s_mov_b32 m0, s7
	s_nop 0
	global_load_lds_dwordx4 v224, s[2:3]
	s_mov_b32 m0, s8
	s_add_i32 s7, s6, 64
	s_lshl_b32 s21, s7, 9
	v_or_b32_e32 v3, s7, v5
	s_add_i32 s7, s21, 0
	v_lshl_add_u32 v225, v3, 4, v2
	s_mov_b32 s8, m0
	s_mov_b32 m0, s7
	s_nop 0
	global_load_lds_dwordx4 v225, s[2:3]
	s_mov_b32 m0, s8
	s_add_i32 s7, s6, 0x50
	s_lshl_b32 s22, s7, 9
	v_or_b32_e32 v3, s7, v5
	s_add_i32 s7, s22, 0
	v_lshl_add_u32 v226, v3, 4, v2
	s_mov_b32 s8, m0
	s_mov_b32 m0, s7
	s_nop 0
	global_load_lds_dwordx4 v226, s[2:3]
	s_mov_b32 m0, s8
	s_add_i32 s7, s6, 0x60
	v_or_b32_e32 v3, s7, v5
	s_addk_i32 s6, 0x70
	v_and_b32_e32 v1, 31, v0
	v_lshl_add_u32 v227, v3, 4, v2
	s_lshl_b32 s23, s7, 9
	v_or_b32_e32 v3, s6, v5
	s_lshl_b32 s24, s6, 9
	s_add_i32 s7, s23, 0
	s_mov_b32 s8, m0
	s_mov_b32 m0, s7
	s_nop 0
	global_load_lds_dwordx4 v227, s[2:3]
	s_mov_b32 m0, s8
	v_lshl_add_u32 v228, v3, 4, v2
	s_add_i32 s6, s24, 0
	v_or_b32_e32 v2, s0, v1
	s_mov_b32 s7, m0
	s_mov_b32 m0, s6
	s_nop 0
	global_load_lds_dwordx4 v228, s[2:3]
	s_mov_b32 m0, s7
	s_add_u32 s2, s14, 0x100000
	v_ashrrev_i32_e32 v3, 31, v2
	s_addc_u32 s3, s15, 0
	v_lshlrev_b64 v[2:3], 6, v[2:3]
	v_lshrrev_b32_e32 v4, 3, v0
	v_lshl_add_u64 v[2:3], s[2:3], 0, v[2:3]
	v_and_b32_e32 v148, 60, v4
	v_mov_b32_e32 v149, 0
	v_lshl_add_u64 v[2:3], v[2:3], 0, v[148:149]
	global_load_dword v6, v[2:3], off
	v_lshlrev_b32_e32 v2, 4, v5
	v_mov_b32_e32 v3, v149
	s_mov_b64 s[6:7], 0x300000
	v_lshl_add_u64 v[2:3], s[14:15], 0, v[2:3]
	v_lshl_add_u64 v[150:151], v[2:3], 0, s[6:7]
	s_lshr_b32 s7, s13, 31
	s_mov_b64 s[8:9], 0x65100000
	s_add_i32 s6, 0, 0x20400
	s_add_i32 s13, s13, s7
	v_and_b32_e32 v7, 0x1e0, v0
	v_lshl_add_u64 v[152:153], v[2:3], 0, s[8:9]
	v_lshl_add_u32 v2, v0, 2, s6
	v_lshl_add_u64 v[154:155], s[2:3], 0, v[148:149]
	s_lshl_b32 s2, s13, 5
	s_mul_i32 s12, s12, s10
	s_andn2_b32 s2, s2, 63
	v_lshlrev_b32_e32 v3, 2, v1
	v_lshlrev_b32_e32 v8, 4, v1
	s_sub_i32 s27, s11, s12
	s_lshl_b32 s26, s26, 7
	s_add_i32 s28, s2, 64
	v_lshlrev_b32_e32 v4, 2, v5
	s_add_u32 s2, s14, 0x31500000
	s_mov_b32 s25, 0
	s_addc_u32 s3, s15, 0
	v_lshlrev_b32_e32 v148, 2, v4
	s_waitcnt vmcnt(0)
	ds_write_b32 v2, v6
	v_lshlrev_b32_e32 v2, 2, v7
	v_add3_u32 v229, s6, v2, v3
	v_lshlrev_b32_e32 v2, 9, v5
	v_add3_u32 v230, 0, v8, v2
	v_add_u32_e32 v2, 0, v3
	v_add_u32_e32 v231, 0x20480, v2
	s_mov_b32 s98, 0
	s_mov_b32 s99, 0
	s_branch .LBB0_648

; __global__ void __launch_bounds__(NTHREADS, 2) mega_fwd(Args args) {
;     ...
;             const int kb0 = seg * 1024 + wave * 128; const bool act = kb0 < nadm;
;             bf16x8 kf[4][4], qlf[4];
;             if (act) {
; #pragma unroll
;                 for (int j = 0; j < 4; ++j)
; #pragma unroll
;                     for (int ks = 0; ks < 4; ++ks) kf[j][ks] = *(const bf16x8*)(KI + (size_t)(kb0 + 32 * j + r32) * IDD + ks * 16 + hi5 * 8);
; #pragma unroll
;                 for (int ks = 0; ks < 4; ++ks) qlf[ks] = *(const bf16x8*)(QLIN + (size_t)(q0 + r32) * IDD + ks * 16 + hi5 * 8);
;             }
.LBB0_648:
	s_lshl_b32 s6, s27, 10
	s_add_i32 s6, s6, s26
	s_cmp_lt_i32 s6, s28
	v_add_u32_e32 v156, s0, v1
	s_cselect_b64 s[14:15], -1, 0
	s_cmp_ge_i32 s6, s28
	v_ashrrev_i32_e32 v157, 31, v156
	s_cbranch_scc1 .LBB0_650
	s_cmp_lg_u32 s98, 0
	s_cbranch_scc1 .LBB0_650
	v_or_b32_e32 v2, s6, v1
	v_ashrrev_i32_e32 v3, 31, v2
	v_lshlrev_b64 v[4:5], 7, v[2:3]
	v_lshl_add_u64 v[4:5], v[150:151], 0, v[4:5]
	global_load_dwordx4 v[66:69], v[4:5], off
	global_load_dwordx4 v[70:73], v[4:5], off offset:32
	global_load_dwordx4 v[74:77], v[4:5], off offset:64
	global_load_dwordx4 v[78:81], v[4:5], off offset:96
	v_or_b32_e32 v4, 32, v2
	v_ashrrev_i32_e32 v5, 31, v4
	v_lshlrev_b64 v[4:5], 7, v[4:5]
	v_lshl_add_u64 v[4:5], v[150:151], 0, v[4:5]
	global_load_dwordx4 v[82:85], v[4:5], off
	global_load_dwordx4 v[86:89], v[4:5], off offset:32
	global_load_dwordx4 v[90:93], v[4:5], off offset:64
	global_load_dwordx4 v[94:97], v[4:5], off offset:96
	v_or_b32_e32 v4, 64, v2
	v_or_b32_e32 v2, 0x60, v2
	v_ashrrev_i32_e32 v5, 31, v4
	v_ashrrev_i32_e32 v3, 31, v2
	v_lshlrev_b64 v[4:5], 7, v[4:5]
	v_lshlrev_b64 v[2:3], 7, v[2:3]
	v_lshl_add_u64 v[4:5], v[150:151], 0, v[4:5]
	v_lshl_add_u64 v[2:3], v[150:151], 0, v[2:3]
	global_load_dwordx4 v[98:101], v[4:5], off
	global_load_dwordx4 v[102:105], v[4:5], off offset:32
	global_load_dwordx4 v[106:109], v[4:5], off offset:64
	global_load_dwordx4 v[114:117], v[4:5], off offset:96
	global_load_dwordx4 v[130:133], v[2:3], off
	global_load_dwordx4 v[134:137], v[2:3], off offset:32
	global_load_dwordx4 v[138:141], v[2:3], off offset:64
	global_load_dwordx4 v[142:145], v[2:3], off offset:96
	v_lshlrev_b64 v[2:3], 7, v[156:157]
	v_lshl_add_u64 v[2:3], v[152:153], 0, v[2:3]
	global_load_dwordx4 v[110:113], v[2:3], off
	global_load_dwordx4 v[118:121], v[2:3], off offset:32
	global_load_dwordx4 v[122:125], v[2:3], off offset:64
	global_load_dwordx4 v[126:129], v[2:3], off offset:96
.LBB0_650:
	v_readlane_b32 s7, v241, 42
	s_add_i32 s29, s29, s7
	s_cmp_lg_u32 s99, 0
	s_cbranch_scc0 .Lidx_top_w0
	s_waitcnt vmcnt(14)
	s_branch .Lidx_top_w1

; #define VM_WAIT() asm volatile("s_waitcnt vmcnt(0)" ::: "memory")
; __global__ void __launch_bounds__(NTHREADS, 2) mega_fwd(Args args) {
;     ...
;             VM_WAIT();
;             __syncthreads();
;             const int nit = it + F.G; const bool has_next = nit < NITEM; int nq0 = 0, nseg2 = 0, nnadm = 0; float wn = 0.f;
.Lidx_top_w1:
	s_mov_b32 s98, 0
	s_mov_b32 s99, 0
	s_cmpk_lt_i32 s29, 0x480
	s_cselect_b64 s[10:11], -1, 0
	s_cmpk_gt_i32 s29, 0x47f
	s_cselect_b64 s[8:9], -1, 0
	s_and_b64 vcc, exec, s[8:9]
	s_waitcnt lgkmcnt(0)
	s_barrier
	s_cbranch_vccnz .LBB0_654
	s_mov_b32 s7, -1
	s_mov_b32 s12, 32

; #define LAS __attribute__((address_space(3)))
; #define IDX_ACC(cc, jj) do { float s0 = fmaf(wh, __builtin_fabsf(cc[0]), sacc[jj][0]); sacc[jj][0] = s0; \
;                             _Pragma("unroll") for (int r = 1; r < 16; ++r) { float a_ = sacc[jj][r]; asm("v_fma_f32 %0, %1, |%2|, %0" : "+v"(a_) : "v"(wh), "v"(cc[r]), "v"(s0)); sacc[jj][r] = a_; } } while (0)
; __global__ void __launch_bounds__(NTHREADS, 2) mega_fwd(Args args) {
;     ...
;                 for (int h = 0; h < NIH; ++h) {
;                     bf16x8 qf[4];
; #pragma unroll
;                     for (int ks = 0; ks < 4; ++ks) qf[ks] = *(const LAS bf16x8*)(Qs + (((h * 4 + ks) * 2 + hi5) * 32 + r32) * 16);
;                     const float wh = Ws[h * 32 + r32];
; #pragma unroll
;                     for (int jp = 0; jp < 4; jp += 2) { f32x16 c0 = f32x16{}, c1 = f32x16{};
; #pragma unroll
;                         for (int ks = 0; ks < 4; ++ks) { c0 = __builtin_amdgcn_mfma_f32_32x32x16_bf16(kf[jp][ks], qf[ks], c0, 0, 0, 0); c1 = __builtin_amdgcn_mfma_f32_32x32x16_bf16(kf[jp + 1][ks], qf[ks], c1, 0, 0, 0); }
;                         __builtin_amdgcn_sched_barrier(0);
;     ...
;                         IDX_ACC(c0, jp); IDX_ACC(c1, jp + 1);
.LBB0_656:
	v_add_u32_e32 v58, s7, v233
	ds_read_b128 v[42:45], v58
	ds_read_b128 v[46:49], v58 offset:1024
	ds_read_b128 v[50:53], v58 offset:2048
	ds_read_b128 v[54:57], v58 offset:3072
	s_nop 4
	v_add_u32_e32 v2, 0xffffff80, v234
	ds_read_b32 v235, v2
	s_waitcnt lgkmcnt(4)
	v_mfma_f32_32x32x16_bf16 v[10:25], v[66:69], v[42:45], 0
	s_waitcnt lgkmcnt(3)
	v_mfma_f32_32x32x16_bf16 v[10:25], v[70:73], v[46:49], v[10:25]
	s_waitcnt lgkmcnt(2)
	v_mfma_f32_32x32x16_bf16 v[10:25], v[74:77], v[50:53], v[10:25]
	s_waitcnt lgkmcnt(1)
	v_mfma_f32_32x32x16_bf16 v[10:25], v[78:81], v[54:57], v[10:25]
	v_mfma_f32_32x32x16_bf16 v[26:41], v[82:85], v[42:45], 0
	s_waitcnt lgkmcnt(0)
	s_nop 8
	v_fma_f32 v206, v235, |v10|, v206
	v_fma_f32 v207, v235, |v11|, v207
	v_fma_f32 v208, v235, |v12|, v208
	v_fma_f32 v209, v235, |v13|, v209
	v_fma_f32 v210, v235, |v14|, v210
	v_fma_f32 v211, v235, |v15|, v211
	v_fma_f32 v212, v235, |v16|, v212
	v_mfma_f32_32x32x16_bf16 v[26:41], v[86:89], v[46:49], v[26:41]
	v_fma_f32 v213, v235, |v17|, v213
	v_fma_f32 v214, v235, |v18|, v214
	v_fma_f32 v215, v235, |v19|, v215
	v_fma_f32 v216, v235, |v20|, v216
	v_fma_f32 v217, v235, |v21|, v217
	v_fma_f32 v218, v235, |v22|, v218
	v_fma_f32 v219, v235, |v23|, v219
	v_mfma_f32_32x32x16_bf16 v[4:19], v[98:101], v[42:45], 0
	v_fma_f32 v220, v235, |v24|, v220
	v_fma_f32 v221, v235, |v25|, v221
	v_mfma_f32_32x32x16_bf16 v[26:41], v[90:93], v[50:53], v[26:41]
	v_mfma_f32_32x32x16_bf16 v[4:19], v[102:105], v[46:49], v[4:19]
	v_mfma_f32_32x32x16_bf16 v[26:41], v[94:97], v[54:57], v[26:41]
	v_mfma_f32_32x32x16_bf16 v[4:19], v[106:109], v[50:53], v[4:19]
	s_nop 9
	v_fma_f32 v190, v235, |v26|, v190
	v_fma_f32 v191, v235, |v27|, v191
	v_fma_f32 v192, v235, |v28|, v192
	v_fma_f32 v193, v235, |v29|, v193
	v_fma_f32 v194, v235, |v30|, v194
	v_fma_f32 v195, v235, |v31|, v195
	v_fma_f32 v196, v235, |v32|, v196
	v_fma_f32 v197, v235, |v33|, v197
	v_fma_f32 v198, v235, |v34|, v198
	v_fma_f32 v199, v235, |v35|, v199
	v_fma_f32 v200, v235, |v36|, v200
	v_fma_f32 v201, v235, |v37|, v201
	v_fma_f32 v202, v235, |v38|, v202
	v_fma_f32 v203, v235, |v39|, v203
	v_fma_f32 v204, v235, |v40|, v204
	v_fma_f32 v205, v235, |v41|, v205
	v_mfma_f32_32x32x16_bf16 v[4:19], v[114:117], v[54:57], v[4:19]
	v_mfma_f32_32x32x16_bf16 v[20:35], v[130:133], v[42:45], 0
	s_nop 9
	v_fma_f32 v188, v235, |v4|, v188
	v_fma_f32 v189, v235, |v5|, v189
	v_fma_f32 v186, v235, |v6|, v186
	v_fma_f32 v187, v235, |v7|, v187
	v_fma_f32 v184, v235, |v8|, v184
	v_fma_f32 v185, v235, |v9|, v185
	v_fma_f32 v182, v235, |v10|, v182
	v_mfma_f32_32x32x16_bf16 v[20:35], v[134:137], v[46:49], v[20:35]
	v_fma_f32 v183, v235, |v11|, v183
	v_fma_f32 v180, v235, |v12|, v180
	v_fma_f32 v181, v235, |v13|, v181
	v_fma_f32 v178, v235, |v14|, v178
	v_fma_f32 v179, v235, |v15|, v179
	v_fma_f32 v176, v235, |v16|, v176
	v_fma_f32 v177, v235, |v17|, v177
	v_mfma_f32_32x32x16_bf16 v[20:35], v[138:141], v[50:53], v[20:35]
	ds_read_b128 v[50:53], v58 offset:4096
	ds_read_b128 v[62:65], v58 offset:6144
	v_fma_f32 v174, v235, |v18|, v174
	v_fma_f32 v175, v235, |v19|, v175
	v_mfma_f32_32x32x16_bf16 v[20:35], v[142:145], v[54:57], v[20:35]
	ds_read_b128 v[54:57], v58 offset:5120
	ds_read_b128 v[58:61], v58 offset:7168
	s_waitcnt lgkmcnt(3)
	v_mfma_f32_32x32x16_bf16 v[2:17], v[66:69], v[50:53], 0
	s_nop 7
	v_fma_f32 v172, v235, |v20|, v172
	v_fma_f32 v173, v235, |v21|, v173
	v_fma_f32 v170, v235, |v22|, v170
	v_fma_f32 v171, v235, |v23|, v171
	v_fma_f32 v168, v235, |v24|, v168
	v_fma_f32 v169, v235, |v25|, v169
	v_fma_f32 v166, v235, |v26|, v166
	s_waitcnt lgkmcnt(1)
	v_mfma_f32_32x32x16_bf16 v[2:17], v[70:73], v[54:57], v[2:17]
	v_fma_f32 v167, v235, |v27|, v167
	v_fma_f32 v164, v235, |v28|, v164
	v_fma_f32 v165, v235, |v29|, v165
	v_fma_f32 v162, v235, |v30|, v162
	v_fma_f32 v163, v235, |v31|, v163
	v_fma_f32 v160, v235, |v32|, v160
	v_fma_f32 v161, v235, |v33|, v161
	v_mfma_f32_32x32x16_bf16 v[2:17], v[74:77], v[62:65], v[2:17]
	v_fma_f32 v158, v235, |v34|, v158
	v_fma_f32 v159, v235, |v35|, v159
	ds_read_b32 v235, v234
	s_waitcnt lgkmcnt(1)
	v_mfma_f32_32x32x16_bf16 v[2:17], v[78:81], v[58:61], v[2:17]
	v_mfma_f32_32x32x16_bf16 v[34:49], v[82:85], v[50:53], 0
	s_waitcnt lgkmcnt(0)
; #define LAS __attribute__((address_space(3)))
; #define IDX_ACC(cc, jj) do { float s0 = fmaf(wh, __builtin_fabsf(cc[0]), sacc[jj][0]); sacc[jj][0] = s0; \
;                             _Pragma("unroll") for (int r = 1; r < 16; ++r) { float a_ = sacc[jj][r]; asm("v_fma_f32 %0, %1, |%2|, %0" : "+v"(a_) : "v"(wh), "v"(cc[r]), "v"(s0)); sacc[jj][r] = a_; } } while (0)
; __global__ void __launch_bounds__(NTHREADS, 2) mega_fwd(Args args) {
;     ...
;                 for (int h = 0; h < NIH; ++h) {
;                     bf16x8 qf[4];
; #pragma unroll
;                     for (int ks = 0; ks < 4; ++ks) qf[ks] = *(const LAS bf16x8*)(Qs + (((h * 4 + ks) * 2 + hi5) * 32 + r32) * 16);
;                     const float wh = Ws[h * 32 + r32];
; #pragma unroll
;                     for (int jp = 0; jp < 4; jp += 2) { f32x16 c0 = f32x16{}, c1 = f32x16{};
; #pragma unroll
;                         for (int ks = 0; ks < 4; ++ks) { c0 = __builtin_amdgcn_mfma_f32_32x32x16_bf16(kf[jp][ks], qf[ks], c0, 0, 0, 0); c1 = __builtin_amdgcn_mfma_f32_32x32x16_bf16(kf[jp + 1][ks], qf[ks], c1, 0, 0, 0); }
;                         __builtin_amdgcn_sched_barrier(0);
;     ...
;                         IDX_ACC(c0, jp); IDX_ACC(c1, jp + 1);
;     ...
;                     }
;                 }
; #pragma unroll
;                 for (int j = 0; j < 4; ++j) { f32x16 c = f32x16{};
; #pragma unroll
;                     for (int ks = 0; ks < 4; ++ks) c = __builtin_amdgcn_mfma_f32_32x32x16_bf16(kf[j][ks], qlf[ks], c, 0, 0, 0);
; #pragma unroll
;                     for (int r = 0; r < 16; ++r) sacc[j][r] = 0.5f * (sacc[j][r] + c[r]); }
;                 float* srow = SCORES + (size_t)(q0 + r32) * S;
; #pragma unroll
;                 for (int j = 0; j < 4; ++j) if (kb0 + 32 * j < nadm) {
; #pragma unroll
;                     for (int rg = 0; rg < 4; ++rg) *(f32x4*)(srow + kb0 + 32 * j + 8 * rg + 4 * hi5) = (f32x4){sacc[j][4 * rg], sacc[j][4 * rg + 1], sacc[j][4 * rg + 2], sacc[j][4 * rg + 3]}; }
;             }
;             if (has_next) { Wsb[(buf ^ 1) * 512 + (tid >> 5) * 32 + (tid & 31)] = wn; q0 = nq0; seg = nseg2; nadm = nnadm; buf ^= 1; }
	s_nop 9
	v_fma_f32 v206, v235, |v2|, v206
	v_fma_f32 v207, v235, |v3|, v207
	v_fma_f32 v208, v235, |v4|, v208
	v_fma_f32 v209, v235, |v5|, v209
	v_fma_f32 v210, v235, |v6|, v210
	v_fma_f32 v211, v235, |v7|, v211
	v_fma_f32 v212, v235, |v8|, v212
	v_mfma_f32_32x32x16_bf16 v[34:49], v[86:89], v[54:57], v[34:49]
	v_fma_f32 v213, v235, |v9|, v213
	v_fma_f32 v214, v235, |v10|, v214
	v_fma_f32 v215, v235, |v11|, v215
	v_fma_f32 v216, v235, |v12|, v216
	v_fma_f32 v217, v235, |v13|, v217
	v_fma_f32 v218, v235, |v14|, v218
	v_fma_f32 v219, v235, |v15|, v219
	v_mfma_f32_32x32x16_bf16 v[18:33], v[98:101], v[50:53], 0
	v_fma_f32 v220, v235, |v16|, v220
	v_fma_f32 v221, v235, |v17|, v221
	v_mfma_f32_32x32x16_bf16 v[34:49], v[90:93], v[62:65], v[34:49]
	v_mfma_f32_32x32x16_bf16 v[18:33], v[102:105], v[54:57], v[18:33]
	v_mfma_f32_32x32x16_bf16 v[34:49], v[94:97], v[58:61], v[34:49]
	v_mfma_f32_32x32x16_bf16 v[18:33], v[106:109], v[62:65], v[18:33]
	s_nop 10
	v_fma_f32 v190, v235, |v34|, v190
	v_fma_f32 v191, v235, |v35|, v191
	v_fma_f32 v192, v235, |v36|, v192
	v_fma_f32 v193, v235, |v37|, v193
	v_fma_f32 v194, v235, |v38|, v194
	v_fma_f32 v195, v235, |v39|, v195
	v_fma_f32 v196, v235, |v40|, v196
	v_fma_f32 v197, v235, |v41|, v197
	v_fma_f32 v198, v235, |v42|, v198
	v_fma_f32 v199, v235, |v43|, v199
	v_fma_f32 v200, v235, |v44|, v200
	v_fma_f32 v201, v235, |v45|, v201
	v_fma_f32 v202, v235, |v46|, v202
	v_fma_f32 v203, v235, |v47|, v203
	v_fma_f32 v204, v235, |v48|, v204
	v_fma_f32 v205, v235, |v49|, v205
	v_mfma_f32_32x32x16_bf16 v[18:33], v[114:117], v[58:61], v[18:33]
	v_mfma_f32_32x32x16_bf16 v[2:17], v[130:133], v[50:53], 0
	s_addk_i32 s7, 0x2000
	s_nop 9
	v_fma_f32 v188, v235, |v18|, v188
	s_cmp_lg_u32 s7, 0x10000
	v_add_u32_e32 v234, 0x100, v234
	v_fma_f32 v189, v235, |v19|, v189
	v_fma_f32 v186, v235, |v20|, v186
	v_fma_f32 v187, v235, |v21|, v187
	v_mfma_f32_32x32x16_bf16 v[2:17], v[134:137], v[54:57], v[2:17]
	v_fma_f32 v184, v235, |v22|, v184
	v_fma_f32 v185, v235, |v23|, v185
	v_fma_f32 v182, v235, |v24|, v182
	v_fma_f32 v183, v235, |v25|, v183
	v_fma_f32 v180, v235, |v26|, v180
	v_fma_f32 v181, v235, |v27|, v181
	v_fma_f32 v178, v235, |v28|, v178
	v_mfma_f32_32x32x16_bf16 v[2:17], v[138:141], v[62:65], v[2:17]
	v_fma_f32 v179, v235, |v29|, v179
	v_fma_f32 v176, v235, |v30|, v176
	v_fma_f32 v177, v235, |v31|, v177
	v_fma_f32 v174, v235, |v32|, v174
	v_fma_f32 v175, v235, |v33|, v175
	v_mfma_f32_32x32x16_bf16 v[2:17], v[142:145], v[58:61], v[2:17]
	s_nop 11
	v_fma_f32 v172, v235, |v2|, v172
	v_fma_f32 v173, v235, |v3|, v173
	v_fma_f32 v170, v235, |v4|, v170
	v_fma_f32 v171, v235, |v5|, v171
	v_fma_f32 v168, v235, |v6|, v168
	v_fma_f32 v169, v235, |v7|, v169
	v_fma_f32 v166, v235, |v8|, v166
	v_fma_f32 v167, v235, |v9|, v167
	v_fma_f32 v164, v235, |v10|, v164
	v_fma_f32 v165, v235, |v11|, v165
	v_fma_f32 v162, v235, |v12|, v162
	v_fma_f32 v163, v235, |v13|, v163
	v_fma_f32 v160, v235, |v14|, v160
	v_fma_f32 v161, v235, |v15|, v161
	v_fma_f32 v158, v235, |v16|, v158
	v_fma_f32 v159, v235, |v17|, v159
	s_cbranch_scc1 .LBB0_656
	s_xor_b32 s7, s25, 1
	v_lshl_add_u32 v2, s7, 11, v229
	s_waitcnt vmcnt(0)
	ds_write_b32 v2, v232
	v_mfma_f32_32x32x16_bf16 v[50:65], v[66:69], v[110:113], 0
	v_lshlrev_b64 v[2:3], 15, v[156:157]
	v_lshl_add_u64 v[2:3], s[2:3], 0, v[2:3]
	s_ashr_i32 s7, s6, 31
	v_lshl_add_u64 v[2:3], s[6:7], 2, v[2:3]
	v_lshl_add_u64 v[156:157], v[2:3], 0, v[148:149]
	s_or_b32 s7, s6, 32
	s_cmp_ge_i32 s7, s28
	v_mfma_f32_32x32x16_bf16 v[34:49], v[82:85], v[110:113], 0
	v_mfma_f32_32x32x16_bf16 v[18:33], v[98:101], v[110:113], 0
	v_mfma_f32_32x32x16_bf16 v[2:17], v[130:133], v[110:113], 0
	v_mfma_f32_32x32x16_bf16 v[50:65], v[70:73], v[118:121], v[50:65]
	v_mfma_f32_32x32x16_bf16 v[34:49], v[86:89], v[118:121], v[34:49]
	v_mfma_f32_32x32x16_bf16 v[18:33], v[102:105], v[118:121], v[18:33]
	v_mfma_f32_32x32x16_bf16 v[2:17], v[134:137], v[118:121], v[2:17]
	v_mfma_f32_32x32x16_bf16 v[50:65], v[74:77], v[122:125], v[50:65]
	v_mfma_f32_32x32x16_bf16 v[34:49], v[90:93], v[122:125], v[34:49]
	v_mfma_f32_32x32x16_bf16 v[18:33], v[106:109], v[122:125], v[18:33]
	v_mfma_f32_32x32x16_bf16 v[2:17], v[138:141], v[122:125], v[2:17]
	v_mfma_f32_32x32x16_bf16 v[50:65], v[78:81], v[126:129], v[50:65]
	v_mfma_f32_32x32x16_bf16 v[34:49], v[94:97], v[126:129], v[34:49]
	s_nop 10
	v_add_f32_e64 v52, v52, v208
	v_add_f32_e64 v53, v53, v209
	v_add_f32_e64 v50, v50, v206
	v_add_f32_e64 v51, v51, v207
	v_add_f32_e64 v56, v56, v212
	v_add_f32_e64 v57, v57, v213
	v_pk_add_f32 v[54:55], v[54:55], v[210:211]
	v_pk_mul_f32 v[52:53], v[52:53], 0.5 op_sel_hi:[1,0]
	v_pk_mul_f32 v[50:51], v[50:51], 0.5 op_sel_hi:[1,0]
	v_pk_add_f32 v[60:61], v[60:61], v[216:217]
	v_mfma_f32_32x32x16_bf16 v[18:33], v[114:117], v[126:129], v[18:33]
	v_add_f32_e64 v58, v58, v214
	v_add_f32_e64 v59, v59, v215
	global_store_dwordx4 v[156:157], v[50:53], off
	v_add_f32_e64 v64, v64, v220
	v_add_f32_e64 v65, v65, v221
	v_pk_add_f32 v[62:63], v[62:63], v[218:219]
	v_pk_mul_f32 v[52:53], v[56:57], 0.5 op_sel_hi:[1,0]
	v_pk_mul_f32 v[50:51], v[54:55], 0.5 op_sel_hi:[1,0]
	global_store_dwordx4 v[156:157], v[50:53], off offset:32
	v_mfma_f32_32x32x16_bf16 v[2:17], v[142:145], v[126:129], v[2:17]
	s_cmp_eq_u64 s[10:11], 0
	s_cbranch_scc1 .Lidx_nla_skip
; __global__ void __launch_bounds__(NTHREADS, 2) mega_fwd(Args args) {
;     ...
;                     for (int ks = 0; ks < 4; ++ks) kf[j][ks] = *(const bf16x8*)(KI + (size_t)(kb0 + 32 * j + r32) * IDD + ks * 16 + hi5 * 8);
; #pragma unroll
;                 for (int ks = 0; ks < 4; ++ks) qlf[ks] = *(const bf16x8*)(QLIN + (size_t)(q0 + r32) * IDD + ks * 16 + hi5 * 8);
;     ...
;                 float* srow = SCORES + (size_t)(q0 + r32) * S;
; #pragma unroll
;                 for (int j = 0; j < 4; ++j) if (kb0 + 32 * j < nadm) {
; #pragma unroll
;                     for (int rg = 0; rg < 4; ++rg) *(f32x4*)(srow + kb0 + 32 * j + 8 * rg + 4 * hi5) = (f32x4){sacc[j][4 * rg], sacc[j][4 * rg + 1], sacc[j][4 * rg + 2], sacc[j][4 * rg + 3]}; }
	s_lshl_b32 s7, s13, 10
	s_add_i32 s7, s7, s26
	s_cmp_ge_i32 s7, s30
	s_cbranch_scc1 .Lidx_nla_skip
	v_or_b32_e32 v236, s7, v1
	v_ashrrev_i32_e32 v237, 31, v236
	v_lshlrev_b64 v[238:239], 7, v[236:237]
	v_lshl_add_u64 v[238:239], v[150:151], 0, v[238:239]
	global_load_dwordx4 v[66:69], v[238:239], off
	global_load_dwordx4 v[70:73], v[238:239], off offset:32
	global_load_dwordx4 v[74:77], v[238:239], off offset:64
	global_load_dwordx4 v[78:81], v[238:239], off offset:96
	v_or_b32_e32 v238, 32, v236
	v_ashrrev_i32_e32 v239, 31, v238
	v_lshlrev_b64 v[238:239], 7, v[238:239]
	v_lshl_add_u64 v[238:239], v[150:151], 0, v[238:239]
	global_load_dwordx4 v[82:85], v[238:239], off
	global_load_dwordx4 v[86:89], v[238:239], off offset:32
	global_load_dwordx4 v[90:93], v[238:239], off offset:64
	global_load_dwordx4 v[94:97], v[238:239], off offset:96
	v_or_b32_e32 v238, 64, v236
	v_ashrrev_i32_e32 v239, 31, v238
	v_lshlrev_b64 v[238:239], 7, v[238:239]
	v_lshl_add_u64 v[238:239], v[150:151], 0, v[238:239]
	global_load_dwordx4 v[98:101], v[238:239], off
	global_load_dwordx4 v[102:105], v[238:239], off offset:32
	global_load_dwordx4 v[106:109], v[238:239], off offset:64
	global_load_dwordx4 v[114:117], v[238:239], off offset:96
	v_or_b32_e32 v238, 96, v236
	v_ashrrev_i32_e32 v239, 31, v238
	v_lshlrev_b64 v[238:239], 7, v[238:239]
	v_lshl_add_u64 v[238:239], v[150:151], 0, v[238:239]
	global_load_dwordx4 v[130:133], v[238:239], off
	global_load_dwordx4 v[134:137], v[238:239], off offset:32
	global_load_dwordx4 v[138:141], v[238:239], off offset:64
	global_load_dwordx4 v[142:145], v[238:239], off offset:96
	v_add_u32_e32 v238, s12, v1
	v_ashrrev_i32_e32 v239, 31, v238
	v_lshlrev_b64 v[238:239], 7, v[238:239]
	v_lshl_add_u64 v[238:239], v[152:153], 0, v[238:239]
	global_load_dwordx4 v[110:113], v[238:239], off
	global_load_dwordx4 v[118:121], v[238:239], off offset:32
	global_load_dwordx4 v[122:125], v[238:239], off offset:64
	global_load_dwordx4 v[126:129], v[238:239], off offset:96
	s_mov_b32 s98, 1
.Lidx_nla_skip:
	s_or_b32 s7, s6, 32
	s_cmp_ge_i32 s7, s28
	s_nop 0
	v_mul_f32_e64 v52, v60, 0.5
	v_mul_f32_e64 v53, v61, 0.5
	v_mul_f32_e64 v50, v58, 0.5
	v_mul_f32_e64 v51, v59, 0.5
	global_store_dwordx4 v[156:157], v[50:53], off offset:64
	s_nop 1
	v_pk_mul_f32 v[52:53], v[64:65], 0.5 op_sel_hi:[1,0]
	v_pk_mul_f32 v[50:51], v[62:63], 0.5 op_sel_hi:[1,0]
	global_store_dwordx4 v[156:157], v[50:53], off offset:96
	s_cbranch_scc1 .LBB0_663
	v_pk_add_f32 v[36:37], v[36:37], v[192:193]
	v_pk_add_f32 v[34:35], v[34:35], v[190:191]
	v_pk_add_f32 v[40:41], v[40:41], v[196:197]
	v_pk_add_f32 v[38:39], v[38:39], v[194:195]
	v_pk_mul_f32 v[36:37], v[36:37], 0.5 op_sel_hi:[1,0]
	v_pk_mul_f32 v[34:35], v[34:35], 0.5 op_sel_hi:[1,0]
	v_pk_add_f32 v[44:45], v[44:45], v[200:201]
	v_pk_add_f32 v[42:43], v[42:43], v[198:199]
	global_store_dwordx4 v[156:157], v[34:37], off offset:128
	v_pk_add_f32 v[48:49], v[48:49], v[204:205]
	v_pk_add_f32 v[46:47], v[46:47], v[202:203]
	v_pk_mul_f32 v[36:37], v[40:41], 0.5 op_sel_hi:[1,0]
	v_pk_mul_f32 v[34:35], v[38:39], 0.5 op_sel_hi:[1,0]
	global_store_dwordx4 v[156:157], v[34:37], off offset:160
	s_nop 1
	v_pk_mul_f32 v[36:37], v[44:45], 0.5 op_sel_hi:[1,0]
	v_pk_mul_f32 v[34:35], v[42:43], 0.5 op_sel_hi:[1,0]
	global_store_dwordx4 v[156:157], v[34:37], off offset:192
	s_nop 1
	v_pk_mul_f32 v[36:37], v[48:49], 0.5 op_sel_hi:[1,0]
	v_pk_mul_f32 v[34:35], v[46:47], 0.5 op_sel_hi:[1,0]
	global_store_dwordx4 v[156:157], v[34:37], off offset:224
	s_or_b32 s7, s6, 64
	s_cmp_ge_i32 s7, s28
	s_cbranch_scc0 .LBB0_664

; __global__ void __launch_bounds__(NTHREADS, 2) mega_fwd(Args args) {
;     ...
;                 float* srow = SCORES + (size_t)(q0 + r32) * S;
; #pragma unroll
;                 for (int j = 0; j < 4; ++j) if (kb0 + 32 * j < nadm) {
; #pragma unroll
;                     for (int rg = 0; rg < 4; ++rg) *(f32x4*)(srow + kb0 + 32 * j + 8 * rg + 4 * hi5) = (f32x4){sacc[j][4 * rg], sacc[j][4 * rg + 1], sacc[j][4 * rg + 2], sacc[j][4 * rg + 3]}; }
;             }
;             if (has_next) { Wsb[(buf ^ 1) * 512 + (tid >> 5) * 32 + (tid & 31)] = wn; q0 = nq0; seg = nseg2; nadm = nnadm; buf ^= 1; }
.LBB0_660:
	s_mov_b32 s99, 1
	v_pk_add_f32 v[2:3], v[2:3], v[172:173]
	v_pk_add_f32 v[4:5], v[4:5], v[170:171]
	v_pk_add_f32 v[6:7], v[6:7], v[168:169]
	v_pk_add_f32 v[8:9], v[8:9], v[166:167]
	v_pk_mul_f32 v[4:5], v[4:5], 0.5 op_sel_hi:[1,0]
	v_pk_mul_f32 v[2:3], v[2:3], 0.5 op_sel_hi:[1,0]
	v_pk_add_f32 v[10:11], v[10:11], v[164:165]
	v_pk_add_f32 v[12:13], v[12:13], v[162:163]
	global_store_dwordx4 v[156:157], v[2:5], off offset:384
	v_pk_add_f32 v[14:15], v[14:15], v[160:161]
	v_pk_add_f32 v[16:17], v[16:17], v[158:159]
	v_pk_mul_f32 v[4:5], v[8:9], 0.5 op_sel_hi:[1,0]
	v_pk_mul_f32 v[2:3], v[6:7], 0.5 op_sel_hi:[1,0]
	global_store_dwordx4 v[156:157], v[2:5], off offset:416
	s_nop 1
	v_pk_mul_f32 v[4:5], v[12:13], 0.5 op_sel_hi:[1,0]
	v_pk_mul_f32 v[2:3], v[10:11], 0.5 op_sel_hi:[1,0]
	global_store_dwordx4 v[156:157], v[2:5], off offset:448
	s_nop 1
	v_pk_mul_f32 v[4:5], v[16:17], 0.5 op_sel_hi:[1,0]
	v_pk_mul_f32 v[2:3], v[14:15], 0.5 op_sel_hi:[1,0]
	global_store_dwordx4 v[156:157], v[2:5], off offset:480
.LBB0_661:
	s_andn2_b64 vcc, exec, s[10:11]
	s_cbranch_vccnz .LBB0_647
	s_xor_b32 s25, s25, 1
	v_lshl_add_u32 v2, s25, 11, v229
	s_mov_b32 s0, s12
	s_mov_b32 s27, s13
	s_mov_b32 s28, s30
	s_cmp_lg_u64 s[14:15], 0
	s_cbranch_scc1 .Lidx_wsb_done
	s_waitcnt vmcnt(0)
	ds_write_b32 v2, v232
.Lidx_wsb_done:
	s_branch .LBB0_647
.LBB0_663:
	s_or_b32 s7, s6, 64
	s_cmp_ge_i32 s7, s28
	s_cbranch_scc1 .LBB0_659
